# attention loops: fewer VALU ops per KV tile (scalar-base K/V prefetch loads, lazy-rescale fast path skips alpha exp, dead movs and canonicalize ops removed, dedicated all-ones operand); windowed atten
# speedup vs baseline: 1.0111x; 1.0036x over previous
.Lfastjoin_h2:
	v_fma_f32 v122, v150, s4, 1.0
	v_mov_b32_e32 v123, v122
	v_fmamk_f32 v100, v100, 0x3e0293ee, v122
	v_fmamk_f32 v101, v101, 0x3e0293ee, v122
	v_fmamk_f32 v102, v102, 0x3e0293ee, v122
	v_fmamk_f32 v103, v103, 0x3e0293ee, v122
	v_fmamk_f32 v104, v104, 0x3e0293ee, v122
	v_fmamk_f32 v105, v105, 0x3e0293ee, v122
	v_fmamk_f32 v106, v106, 0x3e0293ee, v122
	v_fmamk_f32 v107, v107, 0x3e0293ee, v122
	v_fmamk_f32 v108, v108, 0x3e0293ee, v122
	v_fmamk_f32 v109, v109, 0x3e0293ee, v122
	v_fmamk_f32 v110, v110, 0x3e0293ee, v122
	v_fmamk_f32 v111, v111, 0x3e0293ee, v122
	v_fmamk_f32 v112, v112, 0x3e0293ee, v122
	v_fmamk_f32 v113, v113, 0x3e0293ee, v122
	v_fmamk_f32 v114, v114, 0x3e0293ee, v122
	v_fmac_f32_e32 v123, 0x3e0293ee, v115
	v_exp_f32_e32 v158, v100
	v_exp_f32_e32 v159, v101
	v_exp_f32_e32 v160, v102
	v_exp_f32_e32 v161, v103
	v_exp_f32_e32 v152, v104
	v_exp_f32_e32 v153, v105
	v_exp_f32_e32 v154, v106
	v_exp_f32_e32 v155, v107
	v_exp_f32_e32 v162, v108
	v_exp_f32_e32 v163, v109
	v_exp_f32_e32 v178, v110
	v_exp_f32_e32 v179, v111
	v_exp_f32_e32 v156, v112
	v_exp_f32_e32 v157, v113
	v_exp_f32_e32 v117, v114
	v_exp_f32_e32 v151, v123
	s_add_u32 s36, s36, 0x8000
	v_pk_fma_f32 v[148:149], v[84:85], s[30:31], v[122:123] op_sel_hi:[1,0,0]
	v_pk_fma_f32 v[142:143], v[86:87], s[30:31], v[122:123] op_sel_hi:[1,0,0]
	v_pk_fma_f32 v[140:141], v[88:89], s[30:31], v[122:123] op_sel_hi:[1,0,0]
	v_pk_fma_f32 v[120:121], v[90:91], s[30:31], v[122:123] op_sel_hi:[1,0,0]
	v_pk_fma_f32 v[118:119], v[92:93], s[30:31], v[122:123] op_sel_hi:[1,0,0]
	v_pk_fma_f32 v[146:147], v[94:95], s[30:31], v[122:123] op_sel_hi:[1,0,0]
	v_pk_fma_f32 v[144:145], v[96:97], s[30:31], v[122:123] op_sel_hi:[1,0,0]
	v_pk_fma_f32 v[122:123], v[98:99], s[30:31], v[122:123] op_sel_hi:[1,0,0]
	s_addc_u32 s37, s37, 0
	s_and_b64 vcc, exec, s[42:43]
	s_waitcnt lgkmcnt(0)
	s_barrier
	s_cbranch_vccnz .LBB0_1297
.LBB0_1288:
	ds_read_b128 v[84:87], v201 offset:50176
	ds_read_b128 v[88:91], v203 offset:50176
	ds_read_b128 v[92:95], v201 offset:54272
	ds_read_b128 v[96:99], v203 offset:54272
	ds_read_b128 v[184:187], v204 offset:50176
	ds_read_b128 v[188:191], v205 offset:50176
	ds_read_b128 v[206:209], v204 offset:54272
	ds_read_b128 v[210:213], v205 offset:54272
	v_exp_f32_e32 v118, v118
	s_waitcnt lgkmcnt(6)
	v_mfma_scale_f32_32x32x64_f8f6f4 v[100:115], v[84:91], v[124:131], 0, v226, v226 op_sel_hi:[0,0,0]
	v_exp_f32_e32 v119, v119
	v_exp_f32_e32 v146, v146
	v_exp_f32_e32 v147, v147
	v_exp_f32_e32 v148, v148
	v_exp_f32_e32 v149, v149
	v_exp_f32_e32 v182, v140
	v_exp_f32_e32 v183, v141
	v_exp_f32_e32 v180, v142
	v_exp_f32_e32 v181, v143
	v_exp_f32_e32 v120, v120
	v_exp_f32_e32 v121, v121
	s_waitcnt lgkmcnt(4)
	v_mfma_scale_f32_32x32x64_f8f6f4 v[84:99], v[92:99], v[124:131], 0, v226, v226 op_sel_hi:[0,0,0]
	v_exp_f32_e32 v122, v122
	v_exp_f32_e32 v123, v123
	v_cvt_pk_fp8_f32 v140, v158, v159
	v_cvt_pk_fp8_f32 v141, v162, v163
	v_cvt_pk_fp8_f32 v142, v152, v153
	v_cvt_pk_fp8_f32 v143, v156, v157
	v_cvt_pk_fp8_f32 v140, v160, v161 op_sel:[0,0,1]
	v_cvt_pk_fp8_f32 v141, v178, v179 op_sel:[0,0,1]
	v_cvt_pk_fp8_f32 v142, v154, v155 op_sel:[0,0,1]
	v_cvt_pk_fp8_f32 v143, v117, v151 op_sel:[0,0,1]
	v_permlane32_swap_b32_e32 v140, v141
	s_nop 0
	v_permlane32_swap_b32_e32 v142, v143
	s_waitcnt lgkmcnt(2)
	v_mfma_scale_f32_32x32x64_f8f6f4 v[100:115], v[184:191], v[132:139], v[100:115], v226, v226 op_sel_hi:[0,0,0]
	v_exp_f32_e32 v185, v145
	v_cvt_pk_fp8_f32 v145, v118, v119
	v_exp_f32_e32 v184, v144
	v_cvt_pk_fp8_f32 v144, v148, v149
	v_cvt_pk_fp8_f32 v145, v146, v147 op_sel:[0,0,1]
	v_cvt_pk_fp8_f32 v146, v182, v183
	v_cvt_pk_fp8_f32 v147, v184, v185
	v_cvt_pk_fp8_f32 v144, v180, v181 op_sel:[0,0,1]
	v_cvt_pk_fp8_f32 v146, v120, v121 op_sel:[0,0,1]
	v_cvt_pk_fp8_f32 v147, v122, v123 op_sel:[0,0,1]
	s_waitcnt lgkmcnt(0)
	v_mfma_scale_f32_32x32x64_f8f6f4 v[84:99], v[206:213], v[132:139], v[84:99], v226, v226 op_sel_hi:[0,0,0]
	v_permlane32_swap_b32_e32 v144, v145
	v_permlane32_swap_b32_e32 v146, v147
	s_add_u32 s52, s36, 0x39984000
	s_addc_u32 s53, s37, 0
	s_add_u32 s54, s36, s20
	s_addc_u32 s55, s37, 0
	global_load_dwordx2 v[184:185], v2, s[52:53]
	global_load_dwordx2 v[186:187], v2, s[52:53] offset:256
	global_load_dwordx2 v[178:179], v166, s[54:55]
	global_load_dwordx2 v[180:181], v168, s[54:55]
	ds_read_b64_tr_b16 v[152:153], v197 offset:0
	ds_read_b64_tr_b16 v[154:155], v197 offset:0x800
	ds_read_b64_tr_b16 v[156:157], v197 offset:0x1000
	ds_read_b64_tr_b16 v[158:159], v197 offset:0x1800
	s_waitcnt lgkmcnt(0)
	s_nop 0
	v_mfma_scale_f32_32x32x64_f8f6f4 v[4:19], v[140:147], v[152:159], v[4:19], v226, v226 op_sel_hi:[0,0,0]
	ds_read_b64_tr_b16 v[152:153], v197 offset:0x200
	ds_read_b64_tr_b16 v[154:155], v197 offset:0xa00
	ds_read_b64_tr_b16 v[156:157], v197 offset:0x1200
	ds_read_b64_tr_b16 v[158:159], v197 offset:0x1a00
	s_waitcnt lgkmcnt(0)
	s_nop 0
	v_mfma_scale_f32_32x32x64_f8f6f4 v[52:67], v[140:147], v[152:159], v[52:67], v226, v226 op_sel_hi:[0,0,0]
	ds_read_b64_tr_b16 v[152:153], v197 offset:0x400
	ds_read_b64_tr_b16 v[154:155], v197 offset:0xc00
	ds_read_b64_tr_b16 v[156:157], v197 offset:0x1400
	ds_read_b64_tr_b16 v[158:159], v197 offset:0x1c00
	s_waitcnt lgkmcnt(0)
	s_nop 0
	v_mfma_scale_f32_32x32x64_f8f6f4 v[36:51], v[140:147], v[152:159], v[36:51], v226, v226 op_sel_hi:[0,0,0]
	ds_read_b64_tr_b16 v[152:153], v197 offset:0x600
	ds_read_b64_tr_b16 v[154:155], v197 offset:0xe00
	ds_read_b64_tr_b16 v[156:157], v197 offset:0x1600
	ds_read_b64_tr_b16 v[158:159], v197 offset:0x1e00
	s_waitcnt lgkmcnt(0)
	v_mfma_scale_f32_32x32x64_f8f6f4 v[20:35], v[140:147], v[152:159], v[20:35], v226, v226 op_sel_hi:[0,0,0]
	s_barrier
	s_waitcnt vmcnt(4)
	v_mfma_scale_f32_32x32x64_f8f6f4 v[68:83], v[140:147], v[240:247], v[68:83], v226, v226 op_sel_hi:[0,0,0]
	v_max_f32_e32 v117, v100, v101
	v_max3_f32 v117, v117, v102, v103
	v_max3_f32 v117, v117, v104, v105
	v_max3_f32 v117, v117, v106, v107
	v_max3_f32 v117, v117, v108, v109
	v_max3_f32 v117, v117, v110, v111
	v_max3_f32 v117, v117, v112, v113
	v_max3_f32 v117, v117, v114, v115
	v_max3_f32 v117, v117, v84, v85
	v_max3_f32 v117, v117, v86, v87
	v_max3_f32 v117, v117, v88, v89
	v_max3_f32 v117, v117, v90, v91
	v_max3_f32 v117, v117, v92, v93
	v_max3_f32 v117, v117, v94, v95
	v_max3_f32 v117, v117, v96, v97
	v_max3_f32 v117, v117, v98, v99
	v_mov_b32_e32 v118, v117
	s_nop 1
	v_permlane32_swap_b32_e32 v117, v118
	v_max_f32_e32 v117, v117, v118
	v_sub_f32_e32 v118, v117, v150
	v_cmp_ge_f32_e32 vcc, s19, v118
	s_waitcnt vmcnt(4)
	v_perm_b32 v120, v176, v174, s14
	v_perm_b32 v121, v176, v174, s15
	v_perm_b32 v122, v177, v175, s14
	v_perm_b32 v123, v177, v175, s15
	s_cmp_eq_u64 vcc, exec
	s_cbranch_scc0 .Lslow_h1
	ds_write_b128 v200, v[120:123] offset:1024
	ds_write2st64_b64 v202, v[170:171], v[172:173] offset0:66 offset1:74
	v_mov_b32_e32 v206, v150
	s_branch .Lfastjoin_h1
.Lslow_h1:
	v_max_f32_e32 v117, v150, v117
	v_sub_f32_e32 v118, v150, v117
	v_mul_f32_e32 v118, 0x3e0293ee, v118
	v_exp_f32_e32 v118, v118
	s_mov_b64 s[40:41], 0
	s_nop 0
	v_cmp_gt_f32_e32 vcc, 1.0, v118
	ds_write_b128 v200, v[120:123] offset:1024
	ds_write2st64_b64 v202, v[170:171], v[172:173] offset0:66 offset1:74
	s_cbranch_vccz .LBB0_1292
	s_and_saveexec_b64 s[0:1], s[38:39]
	ds_write_b32 v199, v118 offset:128
	s_or_b64 exec, exec, s[0:1]
	s_waitcnt lgkmcnt(0)
	v_add_u32_e32 v122, v165, v198
	ds_read_b128 v[118:121], v122 offset:224
	ds_read_b128 v[140:143], v122 offset:192
	ds_read_b128 v[144:147], v122 offset:160
	ds_read_b128 v[152:155], v122 offset:128
	s_waitcnt lgkmcnt(3)
	v_pk_mul_f32 v[16:17], v[16:17], v[118:119]
	s_waitcnt lgkmcnt(2)
	v_pk_mul_f32 v[12:13], v[12:13], v[140:141]
	s_waitcnt lgkmcnt(1)
	v_pk_mul_f32 v[8:9], v[8:9], v[144:145]
	v_pk_mul_f32 v[18:19], v[18:19], v[120:121]
	v_pk_mul_f32 v[14:15], v[14:15], v[142:143]
	v_pk_mul_f32 v[10:11], v[10:11], v[146:147]
	s_waitcnt lgkmcnt(0)
	v_pk_mul_f32 v[6:7], v[6:7], v[154:155]
	v_pk_mul_f32 v[4:5], v[4:5], v[152:153]
	v_pk_mul_f32 v[64:65], v[64:65], v[118:119]
	v_pk_mul_f32 v[60:61], v[60:61], v[140:141]
	v_pk_mul_f32 v[56:57], v[56:57], v[144:145]
	v_pk_mul_f32 v[66:67], v[66:67], v[120:121]
	v_pk_mul_f32 v[62:63], v[62:63], v[142:143]
	v_pk_mul_f32 v[58:59], v[58:59], v[146:147]
	v_pk_mul_f32 v[54:55], v[54:55], v[154:155]
	v_pk_mul_f32 v[52:53], v[52:53], v[152:153]
	v_pk_mul_f32 v[48:49], v[48:49], v[118:119]
	v_pk_mul_f32 v[44:45], v[44:45], v[140:141]
	v_pk_mul_f32 v[40:41], v[40:41], v[144:145]
	v_pk_mul_f32 v[50:51], v[50:51], v[120:121]
	v_pk_mul_f32 v[46:47], v[46:47], v[142:143]
	v_pk_mul_f32 v[42:43], v[42:43], v[146:147]
	v_pk_mul_f32 v[38:39], v[38:39], v[154:155]
	v_pk_mul_f32 v[36:37], v[36:37], v[152:153]
	v_pk_mul_f32 v[32:33], v[32:33], v[118:119]
	v_pk_mul_f32 v[28:29], v[28:29], v[140:141]
	v_pk_mul_f32 v[24:25], v[24:25], v[144:145]
	v_pk_mul_f32 v[34:35], v[34:35], v[120:121]
	v_pk_mul_f32 v[30:31], v[30:31], v[142:143]
	v_pk_mul_f32 v[26:27], v[26:27], v[146:147]
	v_pk_mul_f32 v[22:23], v[22:23], v[154:155]
	v_pk_mul_f32 v[20:21], v[20:21], v[152:153]
	v_pk_mul_f32 v[80:81], v[80:81], v[118:119]
	v_pk_mul_f32 v[76:77], v[76:77], v[140:141]
	v_pk_mul_f32 v[72:73], v[72:73], v[144:145]
	v_pk_mul_f32 v[82:83], v[82:83], v[120:121]
	v_pk_mul_f32 v[78:79], v[78:79], v[142:143]
	v_pk_mul_f32 v[74:75], v[74:75], v[146:147]
	v_pk_mul_f32 v[70:71], v[70:71], v[154:155]
	v_pk_mul_f32 v[68:69], v[68:69], v[152:153]

.Lfastjoin_h1:
	v_fma_f32 v117, v206, s4, 1.0
	v_fmamk_f32 v100, v100, 0x3e0293ee, v117
	v_fmamk_f32 v101, v101, 0x3e0293ee, v117
	v_fmamk_f32 v102, v102, 0x3e0293ee, v117
	v_fmamk_f32 v145, v106, 0x3e0293ee, v117
	v_fmamk_f32 v108, v108, 0x3e0293ee, v117
	v_fmamk_f32 v109, v109, 0x3e0293ee, v117
	v_exp_f32_e32 v143, v100
	v_exp_f32_e32 v144, v101
	v_exp_f32_e32 v214, v102
	v_exp_f32_e32 v216, v145
	v_exp_f32_e32 v145, v108
	v_exp_f32_e32 v146, v109
	v_fmamk_f32 v105, v105, 0x3e0293ee, v117
	v_fmamk_f32 v110, v110, 0x3e0293ee, v117
	v_fmamk_f32 v147, v112, 0x3e0293ee, v117
	v_fmamk_f32 v103, v103, 0x3e0293ee, v117
	v_fmamk_f32 v104, v104, 0x3e0293ee, v117
	v_fmamk_f32 v107, v107, 0x3e0293ee, v117
	v_fmamk_f32 v111, v111, 0x3e0293ee, v117
	v_fmamk_f32 v148, v113, 0x3e0293ee, v117
	v_fmamk_f32 v149, v114, 0x3e0293ee, v117
	v_fmamk_f32 v150, v115, 0x3e0293ee, v117
	v_fmamk_f32 v140, v94, 0x3e0293ee, v117
	v_fmamk_f32 v141, v95, 0x3e0293ee, v117
	v_fmamk_f32 v142, v96, 0x3e0293ee, v117
	v_exp_f32_e32 v220, v105
	v_exp_f32_e32 v219, v110
	v_exp_f32_e32 v224, v147
	v_fmamk_f32 v147, v97, 0x3e0293ee, v117
	v_fmamk_f32 v112, v84, 0x3e0293ee, v117
	v_fmamk_f32 v113, v85, 0x3e0293ee, v117
	v_fmamk_f32 v114, v86, 0x3e0293ee, v117
	v_fmamk_f32 v115, v87, 0x3e0293ee, v117
	v_fmamk_f32 v118, v88, 0x3e0293ee, v117
	v_fmamk_f32 v119, v89, 0x3e0293ee, v117
	v_fmamk_f32 v120, v90, 0x3e0293ee, v117
	v_fmamk_f32 v121, v91, 0x3e0293ee, v117
	v_fmamk_f32 v122, v92, 0x3e0293ee, v117
	v_fmamk_f32 v123, v93, 0x3e0293ee, v117
	v_exp_f32_e32 v215, v103
	v_exp_f32_e32 v218, v104
	v_exp_f32_e32 v217, v107
	v_exp_f32_e32 v221, v111
	v_exp_f32_e32 v225, v148
	v_exp_f32_e32 v222, v149
	v_exp_f32_e32 v223, v150
	v_fmamk_f32 v207, v98, 0x3e0293ee, v117
	v_fmac_f32_e32 v117, 0x3e0293ee, v99
	s_waitcnt lgkmcnt(0)
	s_barrier
	ds_read_b128 v[92:95], v201 offset:33792
	ds_read_b128 v[84:87], v201 offset:37888
	ds_read_b128 v[96:99], v203 offset:33792
	ds_read_b128 v[88:91], v203 offset:37888
	ds_read_b128 v[156:159], v204 offset:33792
	ds_read_b128 v[148:151], v204 offset:37888
	ds_read_b128 v[160:163], v205 offset:33792
	ds_read_b128 v[152:155], v205 offset:37888
	v_exp_f32_e32 v230, v112
	v_exp_f32_e32 v231, v113
	v_exp_f32_e32 v232, v114
	v_exp_f32_e32 v233, v115
	v_exp_f32_e32 v118, v118
	v_exp_f32_e32 v119, v119
	s_waitcnt lgkmcnt(5)
	v_mfma_scale_f32_32x32x64_f8f6f4 v[100:115], v[92:99], v[124:131], 0, v226, v226 op_sel_hi:[0,0,0]
	v_exp_f32_e32 v122, v122
	v_exp_f32_e32 v123, v123
	v_exp_f32_e32 v208, v142
	v_exp_f32_e32 v209, v147
	v_exp_f32_e32 v182, v140
	v_exp_f32_e32 v183, v141
	v_cvt_pk_fp8_f32 v140, v143, v144
	v_cvt_pk_fp8_f32 v141, v145, v146
	v_exp_f32_e32 v120, v120
	v_exp_f32_e32 v121, v121
	s_waitcnt lgkmcnt(4)
	v_mfma_scale_f32_32x32x64_f8f6f4 v[84:99], v[84:91], v[124:131], 0, v226, v226 op_sel_hi:[0,0,0]
	v_exp_f32_e32 v207, v207
	v_exp_f32_e32 v117, v117
	v_cvt_pk_fp8_f32 v142, v218, v220
	v_cvt_pk_fp8_f32 v143, v224, v225
	v_cvt_pk_fp8_f32 v144, v230, v231
	v_cvt_pk_fp8_f32 v145, v122, v123
	v_cvt_pk_fp8_f32 v146, v118, v119
	v_cvt_pk_fp8_f32 v147, v208, v209
	v_cvt_pk_fp8_f32 v140, v214, v215 op_sel:[0,0,1]
	v_cvt_pk_fp8_f32 v141, v219, v221 op_sel:[0,0,1]
	v_cvt_pk_fp8_f32 v142, v216, v217 op_sel:[0,0,1]
	v_cvt_pk_fp8_f32 v143, v222, v223 op_sel:[0,0,1]
	s_waitcnt lgkmcnt(1)
	v_mfma_scale_f32_32x32x64_f8f6f4 v[100:115], v[156:163], v[132:139], v[100:115], v226, v226 op_sel_hi:[0,0,0]
	v_cvt_pk_fp8_f32 v144, v232, v233 op_sel:[0,0,1]
	v_cvt_pk_fp8_f32 v145, v182, v183 op_sel:[0,0,1]
	v_cvt_pk_fp8_f32 v146, v120, v121 op_sel:[0,0,1]
	v_cvt_pk_fp8_f32 v147, v207, v117 op_sel:[0,0,1]
	v_permlane32_swap_b32_e32 v140, v141
	v_permlane32_swap_b32_e32 v142, v143
	s_waitcnt lgkmcnt(0)
	v_mfma_scale_f32_32x32x64_f8f6f4 v[84:99], v[148:155], v[132:139], v[84:99], v226, v226 op_sel_hi:[0,0,0]
	v_permlane32_swap_b32_e32 v144, v145
	v_permlane32_swap_b32_e32 v146, v147
	s_add_i32 s49, s49, 2
	s_cmp_ge_u32 s49, s48
	s_cselect_b64 s[42:43], -1, 0
	s_and_b64 vcc, exec, s[42:43]
	s_cbranch_vccnz .LBB0_1294
	s_add_u32 s52, s36, 0x39988000
	s_addc_u32 s53, s37, 0
	s_add_u32 s54, s36, 0x38888000
	s_addc_u32 s55, s37, 0
	global_load_dwordx2 v[174:175], v2, s[52:53]
	global_load_dwordx2 v[176:177], v2, s[52:53] offset:256
	global_load_dwordx2 v[170:171], v166, s[54:55]
	global_load_dwordx2 v[172:173], v168, s[54:55]
.LBB0_1294:
	ds_read_b64_tr_b16 v[148:149], v196 offset:0
	ds_read_b64_tr_b16 v[150:151], v196 offset:0x800
	ds_read_b64_tr_b16 v[152:153], v196 offset:0x1000
	ds_read_b64_tr_b16 v[154:155], v196 offset:0x1800
	s_waitcnt lgkmcnt(0)
	s_nop 0
	v_mfma_scale_f32_32x32x64_f8f6f4 v[4:19], v[140:147], v[148:155], v[4:19], v226, v226 op_sel_hi:[0,0,0]
	ds_read_b64_tr_b16 v[148:149], v196 offset:0x200
	ds_read_b64_tr_b16 v[150:151], v196 offset:0xa00
	ds_read_b64_tr_b16 v[152:153], v196 offset:0x1200
	ds_read_b64_tr_b16 v[154:155], v196 offset:0x1a00
	s_waitcnt lgkmcnt(0)
	s_nop 0
	v_mfma_scale_f32_32x32x64_f8f6f4 v[52:67], v[140:147], v[148:155], v[52:67], v226, v226 op_sel_hi:[0,0,0]
	ds_read_b64_tr_b16 v[148:149], v196 offset:0x400
	ds_read_b64_tr_b16 v[150:151], v196 offset:0xc00
	ds_read_b64_tr_b16 v[152:153], v196 offset:0x1400
	ds_read_b64_tr_b16 v[154:155], v196 offset:0x1c00
	s_waitcnt lgkmcnt(0)
	s_nop 0
	v_mfma_scale_f32_32x32x64_f8f6f4 v[36:51], v[140:147], v[148:155], v[36:51], v226, v226 op_sel_hi:[0,0,0]
	ds_read_b64_tr_b16 v[148:149], v196 offset:0x600
	ds_read_b64_tr_b16 v[150:151], v196 offset:0xe00
	ds_read_b64_tr_b16 v[152:153], v196 offset:0x1600
	ds_read_b64_tr_b16 v[154:155], v196 offset:0x1e00
	s_waitcnt lgkmcnt(0)
	v_mfma_scale_f32_32x32x64_f8f6f4 v[20:35], v[140:147], v[148:155], v[20:35], v226, v226 op_sel_hi:[0,0,0]
	s_barrier
	s_waitcnt vmcnt(4)
	v_mfma_scale_f32_32x32x64_f8f6f4 v[68:83], v[140:147], v[240:247], v[68:83], v226, v226 op_sel_hi:[0,0,0]
	s_nop 1
	v_max_f32_e32 v117, v100, v101
	v_max3_f32 v117, v117, v102, v103
	v_max3_f32 v117, v117, v104, v105
	v_max3_f32 v117, v117, v106, v107
	v_max3_f32 v117, v117, v108, v109
	v_max3_f32 v117, v117, v110, v111
	v_max3_f32 v117, v117, v112, v113
	v_max3_f32 v117, v117, v114, v115
	v_max3_f32 v117, v117, v84, v85
	v_max3_f32 v117, v117, v86, v87
	v_max3_f32 v117, v117, v88, v89
	v_max3_f32 v117, v117, v90, v91
	v_max3_f32 v117, v117, v92, v93
	v_max3_f32 v117, v117, v94, v95
	v_max3_f32 v117, v117, v96, v97
	v_max3_f32 v117, v117, v98, v99
	v_mov_b32_e32 v118, v117
	s_nop 1
	v_permlane32_swap_b32_e32 v117, v118
	v_max_f32_e32 v117, v117, v118
	v_sub_f32_e32 v118, v117, v206
	v_cmp_ge_f32_e32 vcc, s19, v118
	s_waitcnt vmcnt(2)
	v_perm_b32 v120, v186, v184, s14
	v_perm_b32 v121, v186, v184, s15
	v_perm_b32 v122, v187, v185, s14
	v_perm_b32 v123, v187, v185, s15
	s_cmp_eq_u64 vcc, exec
	s_cbranch_scc0 .Lslow_h2
	ds_write_b128 v200, v[120:123] offset:17408
	s_waitcnt vmcnt(0)
	ds_write2st64_b64 v202, v[178:179], v[180:181] offset0:98 offset1:106
	v_mov_b32_e32 v150, v206
	s_branch .Lfastjoin_h2
.Lslow_h2:
	v_max_f32_e32 v117, v206, v117
	v_sub_f32_e32 v118, v206, v117
	v_mul_f32_e32 v118, 0x3e0293ee, v118
	v_exp_f32_e32 v118, v118
	s_mov_b64 s[40:41], 0
	s_nop 0
	v_cmp_gt_f32_e32 vcc, 1.0, v118
	ds_write_b128 v200, v[120:123] offset:17408
	s_waitcnt vmcnt(0)
	ds_write2st64_b64 v202, v[178:179], v[180:181] offset0:98 offset1:106
	s_cbranch_vccz .LBB0_1287
	s_and_saveexec_b64 s[0:1], s[38:39]
	s_cbranch_execz .LBB0_1286
	ds_write_b32 v199, v118 offset:128
	s_branch .LBB0_1286

.LBB0_2357:
	v_mul_f32_e32 v41, 0x41000000, v41
	v_max_f32_e32 v44, v41, v44
	v_cndmask_b32_e32 v148, v44, v41, vcc
	s_mov_b32 s0, 0xbe38aa3b
	v_fma_f32 v44, v148, s0, 1.0
	v_fmamk_f32 v20, v20, 0x3e38aa3b, v44
	v_fmamk_f32 v21, v21, 0x3e38aa3b, v44
	v_fmamk_f32 v22, v22, 0x3e38aa3b, v44
	v_fmamk_f32 v23, v23, 0x3e38aa3b, v44
	v_fmamk_f32 v24, v24, 0x3e38aa3b, v44
	v_fmamk_f32 v25, v25, 0x3e38aa3b, v44
	v_fmamk_f32 v26, v26, 0x3e38aa3b, v44
	v_fmamk_f32 v27, v27, 0x3e38aa3b, v44
	v_fmamk_f32 v28, v28, 0x3e38aa3b, v44
	v_fmamk_f32 v29, v29, 0x3e38aa3b, v44
	v_fmamk_f32 v30, v30, 0x3e38aa3b, v44
	v_fmamk_f32 v31, v31, 0x3e38aa3b, v44
	v_fmamk_f32 v32, v32, 0x3e38aa3b, v44
	v_fmamk_f32 v33, v33, 0x3e38aa3b, v44
	v_fmamk_f32 v34, v34, 0x3e38aa3b, v44
	v_fmamk_f32 v35, v35, 0x3e38aa3b, v44
	v_pk_fma_f32 v[52:53], v[4:5], s[28:29], v[44:45] op_sel_hi:[1,0,0]
	v_and_b32_e32 v139, 63, v40
	v_and_b32_e32 v4, 0x3fffffc0, v40
	v_lshlrev_b32_e32 v5, 4, v40
	v_exp_f32_e32 v110, v20
	v_exp_f32_e32 v111, v21
	v_exp_f32_e32 v108, v22
	v_exp_f32_e32 v109, v23
	v_exp_f32_e32 v100, v24
	v_exp_f32_e32 v102, v25
	v_exp_f32_e32 v98, v26
	v_exp_f32_e32 v99, v27
	v_exp_f32_e32 v112, v28
	v_exp_f32_e32 v113, v29
	v_exp_f32_e32 v101, v30
	v_exp_f32_e32 v103, v31
	v_exp_f32_e32 v106, v32
	v_exp_f32_e32 v107, v33
	v_exp_f32_e32 v104, v34
	v_exp_f32_e32 v105, v35
	v_pk_fma_f32 v[54:55], v[6:7], s[28:29], v[44:45] op_sel_hi:[1,0,0]
	v_lshl_add_u32 v138, v4, 2, 0
	v_lshlrev_b32_e32 v4, 3, v139
	v_and_b32_e32 v5, 0xc0, v5
	v_lshlrev_b32_e32 v6, 1, v40
	v_and_or_b32 v5, v4, 24, v5
	v_and_b32_e32 v6, 32, v6
	v_and_b32_e32 v4, 0x100, v4
	s_waitcnt vmcnt(3)
	v_or3_b32 v125, v5, v6, v4
	s_add_i32 s0, 0, 0x400
	v_pk_fma_f32 v[94:95], v[18:19], s[28:29], v[44:45] op_sel_hi:[1,0,0]
	v_pk_fma_f32 v[92:93], v[16:17], s[28:29], v[44:45] op_sel_hi:[1,0,0]
	v_pk_fma_f32 v[96:97], v[14:15], s[28:29], v[44:45] op_sel_hi:[1,0,0]
	v_pk_fma_f32 v[60:61], v[12:13], s[28:29], v[44:45] op_sel_hi:[1,0,0]
	v_pk_fma_f32 v[58:59], v[10:11], s[28:29], v[44:45] op_sel_hi:[1,0,0]
	v_pk_fma_f32 v[56:57], v[8:9], s[28:29], v[44:45] op_sel_hi:[1,0,0]
	v_add_u32_e32 v145, s0, v125
	s_waitcnt vmcnt(1)
	v_perm_b32 v4, v43, v42, s14
	v_perm_b32 v5, v43, v42, s15
	s_andn2_b64 vcc, exec, s[38:39]
	v_cmp_gt_u32_e64 s[38:39], 32, v139
	v_lshl_add_u32 v140, v136, 2, v138
	ds_write_b64 v143, v[4:5] offset:9216
	s_waitcnt vmcnt(0)
	ds_write_b64 v144, v[38:39] offset:25600
	s_waitcnt lgkmcnt(0)
	s_barrier
	s_cbranch_vccnz .LBB0_2379
	v_add_u32_e32 v4, s3, v136
	v_sub_u32_e32 v4, v4, v124
	v_sub_u32_e32 v4, v4, v126
	v_lshl_add_u64 v[132:133], s[70:71], 0, v[36:37]
	s_add_i32 s0, 0, 0x2400
	v_subrev_u32_e32 v147, s8, v4
	v_mov_b32_e32 v36, 2.0
	v_mov_b32_e32 v4, 0
	v_lshl_add_u64 v[130:131], s[72:73], 0, v[2:3]
	v_lshl_add_u32 v2, v124, 2, v138
	v_add_u32_e32 v146, s0, v125
	s_movk_i32 s3, 0x100
	s_mov_b32 s25, -1
	v_mov_b32_e32 v5, v4
	v_mov_b32_e32 v6, v4
	v_mov_b32_e32 v7, v4
	v_mov_b32_e32 v8, v4
	v_mov_b32_e32 v9, v4
	v_mov_b32_e32 v10, v4
	v_mov_b32_e32 v11, v4
	v_mov_b32_e32 v12, v4
	v_mov_b32_e32 v13, v4
	v_mov_b32_e32 v14, v4
	v_mov_b32_e32 v15, v4
	v_mov_b32_e32 v16, v4
	v_mov_b32_e32 v17, v4
	v_mov_b32_e32 v18, v4
	v_mov_b32_e32 v19, v4
	v_mov_b32_e32 v20, v4
	v_mov_b32_e32 v21, v4
	v_mov_b32_e32 v22, v4
	v_mov_b32_e32 v23, v4
	v_mov_b32_e32 v24, v4
	v_mov_b32_e32 v25, v4
	v_mov_b32_e32 v26, v4
	v_mov_b32_e32 v27, v4
	v_mov_b32_e32 v28, v4
	v_mov_b32_e32 v29, v4
	v_mov_b32_e32 v30, v4
	v_mov_b32_e32 v31, v4
	v_mov_b32_e32 v32, v4
	v_mov_b32_e32 v33, v4
	v_mov_b32_e32 v34, v4
	v_mov_b32_e32 v35, v4
	v_mov_b32_e32 v37, v36
	v_mov_b32_e32 v38, v36
	v_mov_b32_e32 v39, v36
	v_mov_b32_e32 v40, v36
	v_mov_b32_e32 v41, v36
	v_mov_b32_e32 v42, v36
	v_mov_b32_e32 v43, v36
	v_mov_b32_e32 v44, v36
	v_mov_b32_e32 v45, v36
	v_mov_b32_e32 v46, v36
	v_mov_b32_e32 v47, v36
	v_mov_b32_e32 v48, v36
	v_mov_b32_e32 v49, v36
	v_mov_b32_e32 v50, v36
	v_mov_b32_e32 v51, v36
	v_mov_b32_e32 v240, v116
	v_mov_b32_e32 v241, v116
	v_mov_b32_e32 v242, v116
	v_mov_b32_e32 v243, v116
	v_mov_b32_e32 v244, v116
	v_mov_b32_e32 v245, v116
	v_mov_b32_e32 v246, v116
	v_mov_b32_e32 v247, v116
.LBB0_2359:
	s_add_i32 s6, s25, 2
	ds_read_b128 v[62:65], v127 offset:25600
	ds_read_b128 v[150:153], v127 offset:27648
	ds_read_b128 v[66:69], v137 offset:25600
	ds_read_b128 v[154:157], v137 offset:27648
	v_exp_f32_e32 v114, v52
	v_exp_f32_e32 v115, v53
	v_exp_f32_e32 v117, v54
	v_exp_f32_e32 v118, v55
	v_exp_f32_e32 v119, v56
	v_exp_f32_e32 v120, v57
	v_exp_f32_e32 v121, v58
	v_exp_f32_e32 v122, v59
	v_exp_f32_e32 v123, v60
	v_exp_f32_e32 v134, v61
	s_waitcnt lgkmcnt(1)
	v_mfma_scale_f32_32x32x64_f8f6f4 v[68:83], v[62:69], v[84:91], 0, v226, v226 op_sel_hi:[0,0,0]
	v_exp_f32_e32 v158, v92
	v_cvt_pk_fp8_f32 v92, v110, v111
	v_exp_f32_e32 v111, v94
	v_cvt_pk_fp8_f32 v94, v100, v102
	v_exp_f32_e32 v110, v93
	v_exp_f32_e32 v135, v96
	v_exp_f32_e32 v149, v97
	v_exp_f32_e32 v159, v95
	v_cvt_pk_fp8_f32 v94, v98, v99 op_sel:[0,0,1]
	s_waitcnt lgkmcnt(0)
	v_mfma_scale_f32_32x32x64_f8f6f4 v[52:67], v[150:157], v[84:91], 0, v226, v226 op_sel_hi:[0,0,0]
	v_cvt_pk_fp8_f32 v93, v112, v113
	v_cvt_pk_fp8_f32 v95, v106, v107
	v_cvt_pk_fp8_f32 v96, v114, v115
	v_cvt_pk_fp8_f32 v97, v123, v134
	v_cvt_pk_fp8_f32 v98, v119, v120
	v_cvt_pk_fp8_f32 v99, v158, v110
	v_cvt_pk_fp8_f32 v92, v108, v109 op_sel:[0,0,1]
	v_cvt_pk_fp8_f32 v93, v101, v103 op_sel:[0,0,1]
	v_cvt_pk_fp8_f32 v95, v104, v105 op_sel:[0,0,1]
	v_cvt_pk_fp8_f32 v96, v117, v118 op_sel:[0,0,1]
	v_cvt_pk_fp8_f32 v97, v135, v149 op_sel:[0,0,1]
	v_cvt_pk_fp8_f32 v98, v121, v122 op_sel:[0,0,1]
	v_cvt_pk_fp8_f32 v99, v111, v159 op_sel:[0,0,1]
	v_permlane32_swap_b32_e32 v92, v93
	v_permlane32_swap_b32_e32 v94, v95
	v_permlane32_swap_b32_e32 v96, v97
	v_permlane32_swap_b32_e32 v98, v99
	s_add_i32 s0, s25, 4
	s_cmp_lt_i32 s0, s21
	s_cselect_b32 s0, 0, s21
	s_cselect_b32 s1, s12, 0x1000
	s_lshl_b32 s0, s0, 6
	s_sub_i32 s0, s1, s0
	s_add_i32 s0, s3, s0
	s_sub_i32 s0, s0, 64
	s_ashr_i32 s1, s0, 31
	s_lshl_b64 s[0:1], s[0:1], 8
	v_lshl_add_u64 v[100:101], v[130:131], 0, s[0:1]
	v_lshl_add_u64 v[102:103], v[132:133], 0, s[0:1]
	global_load_dword v149, v[100:101], off
	global_load_dword v150, v[100:101], off offset:256
	global_load_dwordx2 v[134:135], v[102:103], off
	ds_read_b64_tr_b16 v[100:101], v145 offset:0
	ds_read_b64_tr_b16 v[102:103], v145 offset:0x400
	ds_read_b64_tr_b16 v[104:105], v145 offset:0x800
	ds_read_b64_tr_b16 v[106:107], v145 offset:0xc00
	ds_read_b64_tr_b16 v[108:109], v145 offset:0x200
	ds_read_b64_tr_b16 v[110:111], v145 offset:0x600
	ds_read_b64_tr_b16 v[112:113], v145 offset:0xa00
	ds_read_b64_tr_b16 v[114:115], v145 offset:0xe00
	s_waitcnt lgkmcnt(0)
	s_cmp_ge_i32 s6, s21
	v_add_u32_e32 v151, s3, v147
	s_cbranch_scc1 .LBB0_2363
	v_readlane_b32 s42, v151, 31
	v_readlane_b32 s43, v151, 32
	s_nop 3
	s_cmpk_ge_i32 s42, 192
	s_cselect_b32 s44, 1, 0
	s_cmpk_le_i32 s43, 389
	s_cselect_b32 s45, 1, 0
	s_and_b32 s44, s44, s45
	s_cmp_lg_u32 s44, 0
	s_cbranch_scc1 .LBB0_2363
	s_cmpk_lt_i32 s43, 133
	s_cbranch_scc1 .Lallinv_h1
	s_cmpk_gt_i32 s42, 448
	s_cbranch_scc0 .Lmask_h1
.Lallinv_h1:
	v_mov_b32_e32 v68, v238
	v_mov_b32_e32 v69, v238
	v_mov_b32_e32 v70, v238
	v_mov_b32_e32 v71, v238
	v_mov_b32_e32 v72, v238
	v_mov_b32_e32 v73, v238
	v_mov_b32_e32 v74, v238
	v_mov_b32_e32 v75, v238
	v_mov_b32_e32 v76, v238
	v_mov_b32_e32 v77, v238
	v_mov_b32_e32 v78, v238
	v_mov_b32_e32 v79, v238
	v_mov_b32_e32 v80, v238
	v_mov_b32_e32 v81, v238
	v_mov_b32_e32 v82, v238
	v_mov_b32_e32 v83, v238
	v_mov_b32_e32 v52, v238
	v_mov_b32_e32 v53, v238
	v_mov_b32_e32 v54, v238
	v_mov_b32_e32 v55, v238
	v_mov_b32_e32 v56, v238
	v_mov_b32_e32 v57, v238
	v_mov_b32_e32 v58, v238
	v_mov_b32_e32 v59, v238
	v_mov_b32_e32 v60, v238
	v_mov_b32_e32 v61, v238
	v_mov_b32_e32 v62, v238
	v_mov_b32_e32 v63, v238
	v_mov_b32_e32 v64, v238
	v_mov_b32_e32 v65, v238
	v_mov_b32_e32 v66, v238
	v_mov_b32_e32 v67, v238
	s_branch .LBB0_2363
.Lmask_h1:
	v_add_u32_e32 v117, 0xfffffe3f, v151
	v_cmp_lt_u32_e32 vcc, s18, v117
	v_add_u32_e32 v117, 0xfffffe5f, v151
	v_cmp_lt_u32_e64 s[40:41], s18, v117
	v_add_u32_e32 v117, 0xfffffe40, v151
	s_movk_i32 s0, 0xfeff
	v_cndmask_b32_e64 v52, v238, v52, s[40:41]
	v_cmp_lt_u32_e64 s[40:41], s18, v117
	v_add_u32_e32 v117, 0xfffffe60, v151
	v_cmp_lt_u32_e64 s[42:43], s18, v117
	v_add_u32_e32 v117, 0xfffffe41, v151
	s_nop 0
	v_cndmask_b32_e64 v53, v238, v53, s[42:43]
	v_cmp_lt_u32_e64 s[42:43], s18, v117
	v_add_u32_e32 v117, 0xfffffe61, v151
	v_cmp_lt_u32_e64 s[44:45], s18, v117
	v_add_u32_e32 v117, 0xfffffe42, v151
	s_nop 0
	v_cndmask_b32_e64 v54, v238, v54, s[44:45]
	v_cmp_lt_u32_e64 s[44:45], s18, v117
	v_add_u32_e32 v117, 0xfffffe62, v151
	v_cmp_lt_u32_e64 s[46:47], s18, v117
	v_add_u32_e32 v117, 0xfffffe47, v151
	s_nop 0
	v_cndmask_b32_e64 v55, v238, v55, s[46:47]
	v_cmp_lt_u32_e64 s[46:47], s18, v117
	v_add_u32_e32 v117, 0xfffffe67, v151
	v_cmp_lt_u32_e64 s[48:49], s18, v117
	v_add_u32_e32 v117, 0xfffffe48, v151
	s_nop 0
	v_cndmask_b32_e64 v56, v238, v56, s[48:49]
	v_cmp_lt_u32_e64 s[48:49], s18, v117
	v_add_u32_e32 v117, 0xfffffe68, v151
	v_cmp_lt_u32_e64 s[50:51], s18, v117
	v_add_u32_e32 v117, 0xfffffe49, v151
	s_nop 0
	v_cndmask_b32_e64 v57, v238, v57, s[50:51]
	v_cmp_lt_u32_e64 s[50:51], s18, v117
	v_add_u32_e32 v117, 0xfffffe69, v151
	v_cmp_lt_u32_e64 s[52:53], s18, v117
	v_add_u32_e32 v117, 0xfffffe4a, v151
	s_nop 0
	v_cndmask_b32_e64 v58, v238, v58, s[52:53]
	v_cmp_lt_u32_e64 s[52:53], s18, v117
	v_add_u32_e32 v117, 0xfffffe6a, v151
	v_cmp_lt_u32_e64 s[54:55], s18, v117
	v_add_u32_e32 v117, 0xfffffe4f, v151
	s_nop 0
	v_cndmask_b32_e64 v59, v238, v59, s[54:55]
	v_cmp_lt_u32_e64 s[54:55], s18, v117
	v_add_u32_e32 v117, 0xfffffe6f, v151
	v_cmp_lt_u32_e64 s[56:57], s18, v117
	v_add_u32_e32 v117, 0xfffffe50, v151
	s_nop 0
	v_cndmask_b32_e64 v60, v238, v60, s[56:57]
	v_cmp_lt_u32_e64 s[56:57], s18, v117
	v_add_u32_e32 v117, 0xfffffe70, v151
	v_cmp_lt_u32_e64 s[58:59], s18, v117
	v_add_u32_e32 v117, 0xfffffe51, v151
	s_nop 0
	v_cndmask_b32_e64 v61, v238, v61, s[58:59]
	v_cmp_lt_u32_e64 s[58:59], s18, v117
	v_add_u32_e32 v117, 0xfffffe71, v151
	v_cmp_lt_u32_e64 s[60:61], s18, v117
	v_add_u32_e32 v117, 0xfffffe52, v151
	s_nop 0
	v_cndmask_b32_e64 v62, v238, v62, s[60:61]
	v_cmp_lt_u32_e64 s[60:61], s18, v117
	v_add_u32_e32 v117, 0xfffffe72, v151
	v_cmp_lt_u32_e64 s[62:63], s18, v117
	v_add_u32_e32 v117, 0xfffffe57, v151
	s_nop 0
	v_cndmask_b32_e64 v63, v238, v63, s[62:63]
	v_cmp_lt_u32_e64 s[62:63], s18, v117
	v_add_u32_e32 v117, 0xfffffe77, v151
	v_cmp_lt_u32_e64 s[64:65], s18, v117
	v_add_u32_e32 v117, 0xfffffe58, v151
	s_nop 0
	v_cndmask_b32_e64 v64, v238, v64, s[64:65]
	v_cmp_lt_u32_e64 s[64:65], s18, v117
	v_add_u32_e32 v117, 0xfffffe78, v151
	v_cmp_lt_u32_e64 s[66:67], s18, v117
	v_add_u32_e32 v117, 0xfffffe59, v151
	s_nop 0
	v_cndmask_b32_e64 v65, v238, v65, s[66:67]
	v_cmp_lt_u32_e64 s[66:67], s18, v117
	v_add_u32_e32 v117, 0xfffffe79, v151
	v_cmp_lt_u32_e64 s[68:69], s18, v117
	v_add_u32_e32 v117, 0xfffffe5a, v151
	s_nop 0
	v_cndmask_b32_e64 v66, v238, v66, s[68:69]
	v_cmp_lt_u32_e64 s[68:69], s18, v117
	v_add_u32_e32 v117, 0xfffffe7a, v151
	v_cmp_gt_u32_e64 s[72:73], s0, v117
	s_and_saveexec_b64 s[0:1], s[72:73]
	s_mov_b32 s8, 0xf149f2ca
	v_mov_b32_e32 v67, s8
	s_or_b64 exec, exec, s[0:1]
	v_cndmask_b32_e32 v68, v238, v68, vcc
	v_cndmask_b32_e64 v69, v238, v69, s[40:41]
	v_cndmask_b32_e64 v70, v238, v70, s[42:43]
	v_cndmask_b32_e64 v71, v238, v71, s[44:45]
	v_cndmask_b32_e64 v72, v238, v72, s[46:47]
	v_cndmask_b32_e64 v73, v238, v73, s[48:49]
	v_cndmask_b32_e64 v74, v238, v74, s[50:51]
	v_cndmask_b32_e64 v75, v238, v75, s[52:53]
	v_cndmask_b32_e64 v76, v238, v76, s[54:55]
	v_cndmask_b32_e64 v77, v238, v77, s[56:57]
	v_cndmask_b32_e64 v78, v238, v78, s[58:59]
	v_cndmask_b32_e64 v79, v238, v79, s[60:61]
	v_cndmask_b32_e64 v80, v238, v80, s[62:63]
	v_cndmask_b32_e64 v81, v238, v81, s[64:65]
	v_cndmask_b32_e64 v82, v238, v82, s[66:67]
	v_cndmask_b32_e64 v83, v238, v83, s[68:69]
.LBB0_2363:
	v_mfma_scale_f32_32x32x64_f8f6f4 v[4:19], v[92:99], v[100:107], v[4:19], v226, v226 op_sel_hi:[0,0,0]
	s_barrier
	s_waitcnt vmcnt(3)
	v_mfma_scale_f32_32x32x64_f8f6f4 v[36:51], v[92:99], v[240:247], v[36:51], v226, v226 op_sel_hi:[0,0,0]
	v_mfma_scale_f32_32x32x64_f8f6f4 v[20:35], v[92:99], v[108:115], v[20:35], v226, v226 op_sel_hi:[0,0,0]
	v_max_f32_e32 v92, v68, v69
	v_max3_f32 v92, v92, v70, v71
	v_max3_f32 v92, v92, v72, v73
	v_max3_f32 v92, v92, v74, v75
	v_max3_f32 v92, v92, v76, v77
	v_max3_f32 v92, v92, v78, v79
	v_max3_f32 v92, v92, v80, v81
	v_max3_f32 v92, v92, v82, v83
	v_max3_f32 v92, v92, v52, v53
	v_max3_f32 v92, v92, v54, v55
	v_max3_f32 v92, v92, v56, v57
	v_max3_f32 v92, v92, v58, v59
	v_max3_f32 v92, v92, v60, v61
	v_max3_f32 v92, v92, v62, v63
	v_max3_f32 v92, v92, v64, v65
	v_max3_f32 v92, v92, v66, v67
	v_mov_b32_e32 v93, v92
	s_nop 1
	v_permlane32_swap_b32_e32 v92, v93
	v_max_f32_e32 v92, v92, v93
	v_sub_f32_e32 v93, v92, v148
	v_cmp_ge_f32_e32 vcc, s17, v93
	v_max_f32_e32 v92, v148, v92
	v_sub_f32_e32 v93, v148, v92
	v_mul_f32_e32 v93, 0x3e38aa3b, v93
	v_exp_f32_e32 v93, v93
	s_cmp_eq_u64 vcc, exec
	s_cselect_b64 s[40:41], -1, 0
	v_perm_b32 v94, v142, v141, s14
	v_cndmask_b32_e64 v93, v93, 1.0, s[40:41]
	v_perm_b32 v95, v142, v141, s15
	v_cmp_gt_f32_e32 vcc, 1.0, v93
	ds_write_b64 v143, v[94:95] offset:1024
	ds_write_b64 v144, v[128:129] offset:17408
	s_cbranch_vccz .LBB0_2367
	s_and_saveexec_b64 s[0:1], s[38:39]
	ds_write_b32 v2, v93 offset:33920
	s_or_b64 exec, exec, s[0:1]
	s_waitcnt lgkmcnt(0)
	ds_read_b128 v[94:97], v140 offset:34016
	ds_read_b128 v[98:101], v140 offset:33984
	ds_read_b128 v[102:105], v140 offset:33952
	ds_read_b128 v[106:109], v140 offset:33920
	s_waitcnt lgkmcnt(3)
	v_pk_mul_f32 v[50:51], v[50:51], v[96:97]
	s_waitcnt lgkmcnt(2)
	v_pk_mul_f32 v[46:47], v[46:47], v[100:101]
	s_waitcnt lgkmcnt(1)
	v_pk_mul_f32 v[42:43], v[42:43], v[104:105]
	s_waitcnt lgkmcnt(0)
	v_pk_mul_f32 v[38:39], v[38:39], v[108:109]
	v_pk_mul_f32 v[48:49], v[48:49], v[94:95]
	v_pk_mul_f32 v[44:45], v[44:45], v[98:99]
	v_pk_mul_f32 v[40:41], v[40:41], v[102:103]
	v_pk_mul_f32 v[36:37], v[36:37], v[106:107]
	v_pk_mul_f32 v[18:19], v[18:19], v[96:97]
	v_pk_mul_f32 v[14:15], v[14:15], v[100:101]
	v_pk_mul_f32 v[10:11], v[10:11], v[104:105]
	v_pk_mul_f32 v[6:7], v[6:7], v[108:109]
	v_pk_mul_f32 v[16:17], v[16:17], v[94:95]
	v_pk_mul_f32 v[12:13], v[12:13], v[98:99]
	v_pk_mul_f32 v[8:9], v[8:9], v[102:103]
	v_pk_mul_f32 v[4:5], v[4:5], v[106:107]
	v_pk_mul_f32 v[34:35], v[34:35], v[96:97]
	v_pk_mul_f32 v[30:31], v[30:31], v[100:101]
	v_pk_mul_f32 v[26:27], v[26:27], v[104:105]
	v_pk_mul_f32 v[22:23], v[22:23], v[108:109]
	v_pk_mul_f32 v[32:33], v[32:33], v[94:95]
	v_pk_mul_f32 v[28:29], v[28:29], v[98:99]
	v_pk_mul_f32 v[24:25], v[24:25], v[102:103]
	v_pk_mul_f32 v[20:21], v[20:21], v[106:107]
.LBB0_2367:
	v_cndmask_b32_e64 v148, v92, v148, s[40:41]
	s_mov_b32 s0, 0xbe38aa3b
	v_fma_f32 v92, v148, s0, 1.0
	v_fmamk_f32 v69, v69, 0x3e38aa3b, v92
	v_fmamk_f32 v71, v71, 0x3e38aa3b, v92
	v_fmamk_f32 v73, v73, 0x3e38aa3b, v92
	v_fmamk_f32 v75, v75, 0x3e38aa3b, v92
	v_fmamk_f32 v78, v78, 0x3e38aa3b, v92
	v_fmamk_f32 v79, v79, 0x3e38aa3b, v92
	v_fmamk_f32 v106, v80, 0x3e38aa3b, v92
	v_fmamk_f32 v107, v81, 0x3e38aa3b, v92
	v_fmamk_f32 v68, v68, 0x3e38aa3b, v92
	v_fmamk_f32 v70, v70, 0x3e38aa3b, v92
	v_fmamk_f32 v72, v72, 0x3e38aa3b, v92
	v_fmamk_f32 v104, v74, 0x3e38aa3b, v92
	v_fmamk_f32 v76, v76, 0x3e38aa3b, v92
	v_fmamk_f32 v77, v77, 0x3e38aa3b, v92
	v_fmamk_f32 v108, v82, 0x3e38aa3b, v92
	v_fmamk_f32 v109, v83, 0x3e38aa3b, v92
	v_fmamk_f32 v80, v52, 0x3e38aa3b, v92
	v_fmamk_f32 v81, v53, 0x3e38aa3b, v92
	v_fmamk_f32 v82, v54, 0x3e38aa3b, v92
	v_fmamk_f32 v83, v55, 0x3e38aa3b, v92
	v_fmamk_f32 v93, v56, 0x3e38aa3b, v92
	v_fmamk_f32 v94, v57, 0x3e38aa3b, v92
	v_fmamk_f32 v95, v58, 0x3e38aa3b, v92
	v_fmamk_f32 v96, v59, 0x3e38aa3b, v92
	v_fmamk_f32 v97, v60, 0x3e38aa3b, v92
	v_fmamk_f32 v98, v61, 0x3e38aa3b, v92
	v_fmamk_f32 v99, v62, 0x3e38aa3b, v92
	v_fmamk_f32 v100, v63, 0x3e38aa3b, v92
	v_fmamk_f32 v101, v64, 0x3e38aa3b, v92
	v_exp_f32_e32 v103, v69
	v_exp_f32_e32 v69, v71
	v_exp_f32_e32 v74, v73
	v_exp_f32_e32 v71, v75
	v_exp_f32_e32 v73, v78
	v_exp_f32_e32 v75, v79
	v_exp_f32_e32 v78, v106
	v_exp_f32_e32 v79, v107
	v_fmamk_f32 v106, v65, 0x3e38aa3b, v92
	v_fmamk_f32 v107, v66, 0x3e38aa3b, v92
	v_fmac_f32_e32 v92, 0x3e38aa3b, v67
	v_exp_f32_e32 v102, v68
	v_exp_f32_e32 v68, v70
	v_exp_f32_e32 v72, v72
	v_exp_f32_e32 v70, v104
	v_exp_f32_e32 v104, v76
	v_exp_f32_e32 v105, v77
	v_exp_f32_e32 v76, v108
	v_exp_f32_e32 v77, v109
	s_waitcnt lgkmcnt(0)
	s_barrier
	v_exp_f32_e32 v112, v97
	v_exp_f32_e32 v98, v98
	v_exp_f32_e32 v80, v80
	v_exp_f32_e32 v81, v81
	v_exp_f32_e32 v108, v93
	v_exp_f32_e32 v109, v94
	v_exp_f32_e32 v101, v101
	v_exp_f32_e32 v106, v106
	v_exp_f32_e32 v110, v95
	v_exp_f32_e32 v111, v96
	v_exp_f32_e32 v113, v99
	v_exp_f32_e32 v114, v92
	v_cvt_pk_fp8_f32 v97, v112, v98
	v_exp_f32_e32 v82, v82
	v_exp_f32_e32 v83, v83
	v_exp_f32_e32 v100, v100
	v_exp_f32_e32 v107, v107
	v_cvt_pk_fp8_f32 v92, v102, v103
	v_cvt_pk_fp8_f32 v93, v104, v105
	v_cvt_pk_fp8_f32 v94, v72, v74
	v_cvt_pk_fp8_f32 v95, v78, v79
	v_cvt_pk_fp8_f32 v96, v80, v81
	v_cvt_pk_fp8_f32 v98, v108, v109
	v_cvt_pk_fp8_f32 v99, v101, v106
	ds_read_b128 v[60:63], v127 offset:17408
	ds_read_b128 v[52:55], v127 offset:19456
	ds_read_b128 v[64:67], v137 offset:17408
	ds_read_b128 v[56:59], v137 offset:19456
	v_cvt_pk_fp8_f32 v92, v68, v69 op_sel:[0,0,1]
	v_cvt_pk_fp8_f32 v93, v73, v75 op_sel:[0,0,1]
	v_cvt_pk_fp8_f32 v94, v70, v71 op_sel:[0,0,1]
	v_cvt_pk_fp8_f32 v95, v76, v77 op_sel:[0,0,1]
	v_cvt_pk_fp8_f32 v96, v82, v83 op_sel:[0,0,1]
	v_cvt_pk_fp8_f32 v97, v113, v100 op_sel:[0,0,1]
	v_cvt_pk_fp8_f32 v98, v110, v111 op_sel:[0,0,1]
	v_cvt_pk_fp8_f32 v99, v107, v114 op_sel:[0,0,1]
	v_permlane32_swap_b32_e32 v92, v93
	v_permlane32_swap_b32_e32 v94, v95
	v_permlane32_swap_b32_e32 v96, v97
	v_permlane32_swap_b32_e32 v98, v99
	s_cmp_gt_i32 s6, s21
	s_cselect_b64 s[8:9], -1, 0
	s_and_b64 vcc, exec, s[8:9]
	s_cbranch_vccnz .LBB0_2369
	s_add_i32 s0, s25, 5
	s_cmp_lt_i32 s0, s21
	s_cselect_b32 s0, 0, s21
	s_cselect_b32 s1, s12, 0x1000
	s_lshl_b32 s0, s0, 6
	s_sub_i32 s0, s1, s0
	s_add_i32 s0, s3, s0
	s_ashr_i32 s1, s0, 31
	s_lshl_b64 s[0:1], s[0:1], 8
	v_lshl_add_u64 v[68:69], v[130:131], 0, s[0:1]
	v_lshl_add_u64 v[70:71], v[132:133], 0, s[0:1]
	global_load_dword v141, v[68:69], off
	global_load_dword v142, v[68:69], off offset:256
	global_load_dwordx2 v[128:129], v[70:71], off
.LBB0_2369:
	s_waitcnt lgkmcnt(1)
	v_mfma_scale_f32_32x32x64_f8f6f4 v[68:83], v[60:67], v[84:91], 0, v226, v226 op_sel_hi:[0,0,0]
	s_add_i32 s0, s25, 3
	s_waitcnt lgkmcnt(0)
	v_mfma_scale_f32_32x32x64_f8f6f4 v[52:67], v[52:59], v[84:91], 0, v226, v226 op_sel_hi:[0,0,0]
	ds_read_b64_tr_b16 v[100:101], v146 offset:0
	ds_read_b64_tr_b16 v[102:103], v146 offset:0x400
	ds_read_b64_tr_b16 v[104:105], v146 offset:0x800
	ds_read_b64_tr_b16 v[106:107], v146 offset:0xc00
	ds_read_b64_tr_b16 v[108:109], v146 offset:0x200
	ds_read_b64_tr_b16 v[110:111], v146 offset:0x600
	ds_read_b64_tr_b16 v[112:113], v146 offset:0xa00
	ds_read_b64_tr_b16 v[114:115], v146 offset:0xe00
	s_waitcnt lgkmcnt(0)
	s_cmp_ge_i32 s0, s21
	s_cbranch_scc1 .LBB0_2373
	v_readlane_b32 s42, v151, 31
	v_readlane_b32 s43, v151, 32
	s_nop 3
	s_cmpk_ge_i32 s42, 128
	s_cselect_b32 s44, 1, 0
	s_cmpk_le_i32 s43, 325
	s_cselect_b32 s45, 1, 0
	s_and_b32 s44, s44, s45
	s_cmp_lg_u32 s44, 0
	s_cbranch_scc1 .LBB0_2373
	s_cmpk_lt_i32 s43, 69
	s_cbranch_scc1 .Lallinv_h2
	s_cmpk_gt_i32 s42, 384
	s_cbranch_scc0 .Lmask_h2

.Lmask_h2:
	v_add_u32_e32 v117, 0xfffffe7f, v151
	v_cmp_lt_u32_e32 vcc, s18, v117
	v_add_u32_e32 v117, 0xfffffe9f, v151
	v_cmp_lt_u32_e64 s[40:41], s18, v117
	v_add_u32_e32 v117, 0xfffffe80, v151
	s_movk_i32 s0, 0xfeff
	s_nop 11
	v_cndmask_b32_e64 v52, v238, v52, s[40:41]
	v_cmp_lt_u32_e64 s[40:41], s18, v117
	v_add_u32_e32 v117, 0xfffffea0, v151
	v_cmp_lt_u32_e64 s[42:43], s18, v117
	v_add_u32_e32 v117, 0xfffffe81, v151
	s_nop 0
	v_cndmask_b32_e64 v53, v238, v53, s[42:43]
	v_cmp_lt_u32_e64 s[42:43], s18, v117
	v_add_u32_e32 v117, 0xfffffea1, v151
	v_cmp_lt_u32_e64 s[44:45], s18, v117
	v_add_u32_e32 v117, 0xfffffe82, v151
	s_nop 0
	v_cndmask_b32_e64 v54, v238, v54, s[44:45]
	v_cmp_lt_u32_e64 s[44:45], s18, v117
	v_add_u32_e32 v117, 0xfffffea2, v151
	v_cmp_lt_u32_e64 s[46:47], s18, v117
	v_add_u32_e32 v117, 0xfffffe87, v151
	s_nop 0
	v_cndmask_b32_e64 v55, v238, v55, s[46:47]
	v_cmp_lt_u32_e64 s[46:47], s18, v117
	v_add_u32_e32 v117, 0xfffffea7, v151
	v_cmp_lt_u32_e64 s[48:49], s18, v117
	v_add_u32_e32 v117, 0xfffffe88, v151
	s_nop 0
	v_cndmask_b32_e64 v56, v238, v56, s[48:49]
	v_cmp_lt_u32_e64 s[48:49], s18, v117
	v_add_u32_e32 v117, 0xfffffea8, v151
	v_cmp_lt_u32_e64 s[50:51], s18, v117
	v_add_u32_e32 v117, 0xfffffe89, v151
	s_nop 0
	v_cndmask_b32_e64 v57, v238, v57, s[50:51]
	v_cmp_lt_u32_e64 s[50:51], s18, v117
	v_add_u32_e32 v117, 0xfffffea9, v151
	v_cmp_lt_u32_e64 s[52:53], s18, v117
	v_add_u32_e32 v117, 0xfffffe8a, v151
	s_nop 0
	v_cndmask_b32_e64 v58, v238, v58, s[52:53]
	v_cmp_lt_u32_e64 s[52:53], s18, v117
	v_add_u32_e32 v117, 0xfffffeaa, v151
	v_cmp_lt_u32_e64 s[54:55], s18, v117
	v_add_u32_e32 v117, 0xfffffe8f, v151
	s_nop 0
	v_cndmask_b32_e64 v59, v238, v59, s[54:55]
	v_cmp_lt_u32_e64 s[54:55], s18, v117
	v_add_u32_e32 v117, 0xfffffeaf, v151
	v_cmp_lt_u32_e64 s[56:57], s18, v117
	v_add_u32_e32 v117, 0xfffffe90, v151
	s_nop 0
	v_cndmask_b32_e64 v60, v238, v60, s[56:57]
	v_cmp_lt_u32_e64 s[56:57], s18, v117
	v_add_u32_e32 v117, 0xfffffeb0, v151
	v_cmp_lt_u32_e64 s[58:59], s18, v117
	v_add_u32_e32 v117, 0xfffffe91, v151
	s_nop 0
	v_cndmask_b32_e64 v61, v238, v61, s[58:59]
	v_cmp_lt_u32_e64 s[58:59], s18, v117
	v_add_u32_e32 v117, 0xfffffeb1, v151
	v_cmp_lt_u32_e64 s[60:61], s18, v117
	v_add_u32_e32 v117, 0xfffffe92, v151
	s_nop 0
	v_cndmask_b32_e64 v62, v238, v62, s[60:61]
	v_cmp_lt_u32_e64 s[60:61], s18, v117
	v_add_u32_e32 v117, 0xfffffeb2, v151
	v_cmp_lt_u32_e64 s[62:63], s18, v117
	v_add_u32_e32 v117, 0xfffffe97, v151
	s_nop 0
	v_cndmask_b32_e64 v63, v238, v63, s[62:63]
	v_cmp_lt_u32_e64 s[62:63], s18, v117
	v_add_u32_e32 v117, 0xfffffeb7, v151
	v_cmp_lt_u32_e64 s[64:65], s18, v117
	v_add_u32_e32 v117, 0xfffffe98, v151
	s_nop 0
	v_cndmask_b32_e64 v64, v238, v64, s[64:65]
	v_cmp_lt_u32_e64 s[64:65], s18, v117
	v_add_u32_e32 v117, 0xfffffeb8, v151
	v_cmp_lt_u32_e64 s[66:67], s18, v117
	v_add_u32_e32 v117, 0xfffffe99, v151
	s_nop 0
	v_cndmask_b32_e64 v65, v238, v65, s[66:67]
	v_cmp_lt_u32_e64 s[66:67], s18, v117
	v_add_u32_e32 v117, 0xfffffeb9, v151
	v_cmp_lt_u32_e64 s[68:69], s18, v117
	v_add_u32_e32 v117, 0xfffffe9a, v151
	s_nop 0
	v_cndmask_b32_e64 v66, v238, v66, s[68:69]
	v_cmp_lt_u32_e64 s[68:69], s18, v117
	v_add_u32_e32 v117, 0xfffffeba, v151
	v_cmp_gt_u32_e64 s[72:73], s0, v117
	s_and_saveexec_b64 s[0:1], s[72:73]
	s_mov_b32 s25, 0xf149f2ca
	v_mov_b32_e32 v67, s25
	s_or_b64 exec, exec, s[0:1]
	v_cndmask_b32_e32 v68, v238, v68, vcc
	v_cndmask_b32_e64 v69, v238, v69, s[40:41]
	v_cndmask_b32_e64 v70, v238, v70, s[42:43]
	v_cndmask_b32_e64 v71, v238, v71, s[44:45]
	v_cndmask_b32_e64 v72, v238, v72, s[46:47]
	v_cndmask_b32_e64 v73, v238, v73, s[48:49]
	v_cndmask_b32_e64 v74, v238, v74, s[50:51]
	v_cndmask_b32_e64 v75, v238, v75, s[52:53]
	v_cndmask_b32_e64 v76, v238, v76, s[54:55]
	v_cndmask_b32_e64 v77, v238, v77, s[56:57]
	v_cndmask_b32_e64 v78, v238, v78, s[58:59]
	v_cndmask_b32_e64 v79, v238, v79, s[60:61]
	v_cndmask_b32_e64 v80, v238, v80, s[62:63]
	v_cndmask_b32_e64 v81, v238, v81, s[64:65]
	v_cndmask_b32_e64 v82, v238, v82, s[66:67]
	v_cndmask_b32_e64 v83, v238, v83, s[68:69]
.LBB0_2373:
	v_mfma_scale_f32_32x32x64_f8f6f4 v[4:19], v[92:99], v[100:107], v[4:19], v226, v226 op_sel_hi:[0,0,0]
	s_barrier
	s_waitcnt vmcnt(3)
	v_mfma_scale_f32_32x32x64_f8f6f4 v[36:51], v[92:99], v[240:247], v[36:51], v226, v226 op_sel_hi:[0,0,0]
	v_mfma_scale_f32_32x32x64_f8f6f4 v[20:35], v[92:99], v[108:115], v[20:35], v226, v226 op_sel_hi:[0,0,0]
	s_nop 3
	v_max_f32_e32 v92, v68, v69
	v_max3_f32 v92, v92, v70, v71
	v_max3_f32 v92, v92, v72, v73
	v_max3_f32 v92, v92, v74, v75
	v_max3_f32 v92, v92, v76, v77
	v_max3_f32 v92, v92, v78, v79
	v_max3_f32 v92, v92, v80, v81
	v_max3_f32 v92, v92, v82, v83
	v_max3_f32 v92, v92, v52, v53
	v_max3_f32 v92, v92, v54, v55
	v_max3_f32 v92, v92, v56, v57
	v_max3_f32 v92, v92, v58, v59
	v_max3_f32 v92, v92, v60, v61
	v_max3_f32 v92, v92, v62, v63
	v_max3_f32 v92, v92, v64, v65
	v_max3_f32 v92, v92, v66, v67
	v_mov_b32_e32 v93, v92
	s_nop 1
	v_permlane32_swap_b32_e32 v92, v93
	v_max_f32_e32 v92, v92, v93
	v_sub_f32_e32 v93, v92, v148
	v_cmp_ge_f32_e32 vcc, s17, v93
	v_max_f32_e32 v92, v148, v92
	v_sub_f32_e32 v93, v148, v92
	v_mul_f32_e32 v93, 0x3e38aa3b, v93
	v_exp_f32_e32 v93, v93
	s_cmp_eq_u64 vcc, exec
	s_cselect_b64 s[40:41], -1, 0
	s_waitcnt vmcnt(1)
	v_perm_b32 v94, v150, v149, s14
	v_cndmask_b32_e64 v93, v93, 1.0, s[40:41]
	v_perm_b32 v95, v150, v149, s15
	v_cmp_gt_f32_e32 vcc, 1.0, v93
	ds_write_b64 v143, v[94:95] offset:9216
	s_waitcnt vmcnt(0)
	ds_write_b64 v144, v[134:135] offset:25600
	s_cbranch_vccz .LBB0_2377
	s_and_saveexec_b64 s[0:1], s[38:39]
	ds_write_b32 v2, v93 offset:33920
	s_or_b64 exec, exec, s[0:1]
	s_waitcnt lgkmcnt(0)
	ds_read_b128 v[94:97], v140 offset:34016
	ds_read_b128 v[98:101], v140 offset:33984
	ds_read_b128 v[102:105], v140 offset:33952
	ds_read_b128 v[106:109], v140 offset:33920
	s_waitcnt lgkmcnt(3)
	v_pk_mul_f32 v[50:51], v[50:51], v[96:97]
	s_waitcnt lgkmcnt(2)
	v_pk_mul_f32 v[46:47], v[46:47], v[100:101]
	s_waitcnt lgkmcnt(1)
	v_pk_mul_f32 v[42:43], v[42:43], v[104:105]
	s_waitcnt lgkmcnt(0)
	v_pk_mul_f32 v[38:39], v[38:39], v[108:109]
	v_pk_mul_f32 v[48:49], v[48:49], v[94:95]
	v_pk_mul_f32 v[44:45], v[44:45], v[98:99]
	v_pk_mul_f32 v[40:41], v[40:41], v[102:103]
	v_pk_mul_f32 v[36:37], v[36:37], v[106:107]
	v_pk_mul_f32 v[18:19], v[18:19], v[96:97]
	v_pk_mul_f32 v[14:15], v[14:15], v[100:101]
	v_pk_mul_f32 v[10:11], v[10:11], v[104:105]
	v_pk_mul_f32 v[6:7], v[6:7], v[108:109]
	v_pk_mul_f32 v[16:17], v[16:17], v[94:95]
	v_pk_mul_f32 v[12:13], v[12:13], v[98:99]
	v_pk_mul_f32 v[8:9], v[8:9], v[102:103]
	v_pk_mul_f32 v[4:5], v[4:5], v[106:107]
	v_pk_mul_f32 v[34:35], v[34:35], v[96:97]
	v_pk_mul_f32 v[30:31], v[30:31], v[100:101]
	v_pk_mul_f32 v[26:27], v[26:27], v[104:105]
	v_pk_mul_f32 v[22:23], v[22:23], v[108:109]
	v_pk_mul_f32 v[32:33], v[32:33], v[94:95]
	v_pk_mul_f32 v[28:29], v[28:29], v[98:99]
	v_pk_mul_f32 v[24:25], v[24:25], v[102:103]
	v_pk_mul_f32 v[20:21], v[20:21], v[106:107]
